# baseline (speedup 1.0000x reference)
_Z9k_router2PKfPKDF16_S0_PDF16_PfPiS0_S0_S4_S5_S4_:
	s_lshr_b32 s3, s2, 3
	s_and_b32 s14, s3, 14
	s_movk_i32 s3, 0x200
	v_cmp_gt_u32_e32 vcc, s3, v0
	v_lshlrev_b32_e32 v70, 2, v0
	s_and_saveexec_b64 s[4:5], vcc
	s_xor_b64 s[8:9], exec, s[4:5]
	s_cbranch_execz .LBB0_12
	s_load_dwordx4 s[4:7], s[0:1], 0x8
	s_load_dwordx2 s[10:11], s[0:1], 0x20
	v_and_b32_e32 v1, 63, v0
	s_setprio 1
	v_lshlrev_b32_e32 v2, 7, v0
	v_and_b32_e32 v50, 0xe000, v2
	v_mov_b32_e32 v51, 0
	s_waitcnt lgkmcnt(0)
	v_lshl_add_u64 v[2:3], s[4:5], 0, v[50:51]
	v_lshlrev_b32_e32 v50, 4, v1
	s_mov_b32 s13, 0
	v_lshl_add_u64 v[130:131], v[2:3], 0, v[50:51]
	s_lshl_b32 s12, s14, 16
	v_lshl_add_u64 v[14:15], v[130:131], 0, s[12:13]
	s_movk_i32 s3, 0x1000
	v_add_co_u32_e32 v16, vcc, s3, v14
	s_mov_b32 s4, 0x10000
	s_nop 0
	v_addc_co_u32_e32 v17, vcc, 0, v15, vcc
	v_add_co_u32_e32 v52, vcc, s4, v14
	s_mov_b32 s4, 0x11000
	s_nop 0
	v_addc_co_u32_e32 v53, vcc, 0, v15, vcc
	v_add_co_u32_e32 v72, vcc, s4, v14
	v_and_b32_e32 v1, 15, v0
	s_nop 0
	v_addc_co_u32_e32 v73, vcc, 0, v15, vcc
	global_load_dwordx4 v[54:57], v[14:15], off
	global_load_dwordx4 v[58:61], v[14:15], off offset:1024
	global_load_dwordx4 v[62:65], v[14:15], off offset:2048
	global_load_dwordx4 v[66:69], v[14:15], off offset:3072
	global_load_dwordx4 v[34:37], v[16:17], off
	global_load_dwordx4 v[38:41], v[16:17], off offset:1024
	global_load_dwordx4 v[42:45], v[16:17], off offset:2048
	global_load_dwordx4 v[46:49], v[16:17], off offset:3072
	global_load_dwordx4 v[18:21], v[52:53], off offset:1024
	global_load_dwordx4 v[22:25], v[52:53], off offset:2048
	global_load_dwordx4 v[26:29], v[52:53], off offset:3072
	global_load_dwordx4 v[30:33], v[72:73], off offset:-4096
	global_load_dwordx4 v[2:5], v[72:73], off
	global_load_dwordx4 v[6:9], v[72:73], off offset:1024
	global_load_dwordx4 v[10:13], v[72:73], off offset:2048
	global_load_dwordx4 v[14:17], v[72:73], off offset:3072
	s_lshl_b32 s4, s2, 9
	v_and_b32_e32 v50, 48, v0
	v_lshlrev_b32_e32 v52, 6, v1
	v_and_b32_e32 v53, 32, v70
	s_and_b32 s4, s4, 0xe000
	v_bitop3_b32 v132, v52, v53, v50 bitop3:0x36
	s_addk_i32 s4, 0x7000
	s_mov_b32 s5, -6
	v_mov_b32_e32 v50, v51
	v_mov_b32_e32 v52, v51
	v_mov_b32_e32 v53, v51
	v_mov_b32_e32 v70, v51
	v_mov_b32_e32 v71, v51
	v_mov_b32_e32 v72, v51
	v_mov_b32_e32 v73, v51
	v_mov_b32_e32 v74, v51
	v_mov_b32_e32 v75, v51
	v_mov_b32_e32 v76, v51
	v_mov_b32_e32 v77, v51
	v_mov_b32_e32 v78, v51
	v_mov_b32_e32 v79, v51
	v_mov_b32_e32 v80, v51
	v_mov_b32_e32 v81, v51
	v_mov_b32_e32 v82, v51
	v_mov_b32_e32 v83, v51
	v_mov_b32_e32 v84, v51
	v_mov_b32_e32 v85, v51
	v_mov_b32_e32 v86, v51
	v_mov_b32_e32 v87, v51
	v_mov_b32_e32 v88, v51
	v_mov_b32_e32 v89, v51
	v_mov_b32_e32 v90, v51
	v_mov_b32_e32 v91, v51
	v_mov_b32_e32 v92, v51
	v_mov_b32_e32 v93, v51
	v_mov_b32_e32 v94, v51
	v_mov_b32_e32 v95, v51
	v_mov_b32_e32 v96, v51
	v_mov_b32_e32 v97, v51
	v_mov_b32_e32 v98, v51
	v_mov_b32_e32 v99, v51
	v_mov_b32_e32 v100, v51
	v_mov_b32_e32 v101, v51
	v_mov_b32_e32 v102, v51
	v_mov_b32_e32 v103, v51
	v_mov_b32_e32 v104, v51
	v_mov_b32_e32 v105, v51
	v_mov_b32_e32 v106, v51
	v_mov_b32_e32 v107, v51
	v_mov_b32_e32 v108, v51
	v_mov_b32_e32 v109, v51
	v_mov_b32_e32 v110, v51
	v_mov_b32_e32 v111, v51
	v_mov_b32_e32 v112, v51
	v_mov_b32_e32 v113, v51
	v_mov_b32_e32 v114, v51
	v_mov_b32_e32 v115, v51
	v_mov_b32_e32 v116, v51
	v_mov_b32_e32 v117, v51
	v_mov_b32_e32 v118, v51
	v_mov_b32_e32 v119, v51
	v_mov_b32_e32 v120, v51
	v_mov_b32_e32 v121, v51
	v_mov_b32_e32 v122, v51
	v_mov_b32_e32 v123, v51
	v_mov_b32_e32 v124, v51
	v_mov_b32_e32 v125, v51
	v_mov_b32_e32 v126, v51
	v_mov_b32_e32 v127, v51
	v_mov_b32_e32 v128, v51
	v_mov_b32_e32 v129, v51

.LBB0_12:
	s_andn2_saveexec_b64 s[4:5], s[8:9]
	s_cbranch_execz .LBB0_23
	v_add_u32_e32 v1, 0xfffffe00, v0
	s_load_dwordx2 s[4:5], s[0:1], 0x0
	s_load_dwordx2 s[6:7], s[0:1], 0x18
	v_lshrrev_b32_e32 v78, 4, v1
	v_lshl_add_u32 v68, s2, 6, v78
	v_ashrrev_i32_e32 v69, 31, v68
	v_and_b32_e32 v79, 60, v70
	v_lshlrev_b64 v[2:3], 13, v[68:69]
	s_waitcnt lgkmcnt(0)
	v_lshl_add_u64 v[2:3], s[4:5], 0, v[2:3]
	v_lshlrev_b32_e32 v74, 2, v79
	v_mov_b32_e32 v75, 0
	s_mov_b32 s5, 0
	v_lshl_add_u64 v[66:67], v[2:3], 0, v[74:75]
	s_lshl_b32 s4, s14, 8
	v_lshl_add_u64 v[26:27], v[66:67], 0, s[4:5]
	s_mov_b32 s8, 0x20000
	v_add_co_u32_e32 v28, vcc, s8, v26
	s_lshl_b32 s0, s14, 6
	s_nop 0
	v_addc_co_u32_e32 v29, vcc, 0, v27, vcc
	s_mov_b32 s1, 0x40000
	v_add_co_u32_e32 v38, vcc, s1, v26
	s_add_i32 s4, s0, 0x80
	s_nop 0
	v_addc_co_u32_e32 v39, vcc, 0, v27, vcc
	s_mov_b32 s3, 0x60000
	s_and_b32 s4, s4, 0x780
	v_add_co_u32_e32 v40, vcc, s3, v26
	s_lshl_b32 s4, s4, 2
	s_nop 0
	v_addc_co_u32_e32 v41, vcc, 0, v27, vcc
	v_lshl_add_u64 v[42:43], v[66:67], 0, s[4:5]
	v_add_co_u32_e32 v44, vcc, s8, v42
	s_addk_i32 s0, 0xc0
	s_nop 0
	v_addc_co_u32_e32 v45, vcc, 0, v43, vcc
	v_add_co_u32_e32 v46, vcc, s1, v42
	s_and_b32 s0, s0, 0x7c0
	s_nop 0
	v_addc_co_u32_e32 v47, vcc, 0, v43, vcc
	v_add_co_u32_e32 v48, vcc, s3, v42
	s_lshl_b32 s4, s0, 2
	global_load_dwordx4 v[2:5], v[26:27], off nt
	global_load_dwordx4 v[6:9], v[26:27], off offset:256 nt
	global_load_dwordx4 v[10:13], v[28:29], off nt
	global_load_dwordx4 v[14:17], v[28:29], off offset:256 nt
	global_load_dwordx4 v[18:21], v[38:39], off nt
	global_load_dwordx4 v[22:25], v[38:39], off offset:256 nt
	global_load_dwordx4 v[30:33], v[40:41], off nt
	global_load_dwordx4 v[34:37], v[40:41], off offset:256 nt
	v_addc_co_u32_e32 v49, vcc, 0, v43, vcc
	v_lshl_add_u64 v[58:59], v[66:67], 0, s[4:5]
	v_add_co_u32_e32 v60, vcc, s8, v58
	global_load_dwordx4 v[26:29], v[42:43], off nt
	global_load_dwordx4 v[38:41], v[44:45], off nt
	v_addc_co_u32_e32 v61, vcc, 0, v59, vcc
	v_add_co_u32_e32 v72, vcc, s1, v58
	global_load_dwordx4 v[42:45], v[46:47], off nt
	global_load_dwordx4 v[50:53], v[48:49], off nt
	v_addc_co_u32_e32 v73, vcc, 0, v59, vcc
	v_add_co_u32_e32 v76, vcc, s3, v58
	global_load_dwordx4 v[46:49], v[58:59], off nt
	global_load_dwordx4 v[54:57], v[60:61], off nt
	v_addc_co_u32_e32 v77, vcc, 0, v59, vcc
	global_load_dwordx4 v[58:61], v[72:73], off nt
	global_load_dwordx4 v[62:65], v[76:77], off nt
	v_bfe_u32 v73, v70, 5, 1
	v_lshlrev_b32_e32 v0, 3, v0
	v_lshrrev_b32_e32 v70, 7, v1
	s_mov_b32 s0, 0x3ffffe
	v_and_b32_e32 v0, 56, v0
	v_and_or_b32 v70, v70, s0, v73
	v_lshlrev_b32_e32 v71, 2, v1
	s_movk_i32 s1, 0x3c0
	v_lshrrev_b32_e32 v1, 2, v1
	v_and_or_b32 v71, v71, s1, v0
	v_lshlrev_b32_e32 v70, 10, v70
	v_and_b32_e32 v1, 32, v1
	v_bitop3_b32 v70, v71, v70, v1 bitop3:0xde
	v_add_u32_e32 v1, 16, v78
	v_lshrrev_b32_e32 v71, 3, v1
	v_and_or_b32 v71, v71, s0, v73
	v_lshlrev_b32_e32 v72, 6, v1
	v_lshlrev_b32_e32 v1, 2, v1
	v_and_or_b32 v72, v72, s1, v0
	v_lshlrev_b32_e32 v71, 10, v71
	v_and_b32_e32 v1, 32, v1
	v_bitop3_b32 v71, v72, v71, v1 bitop3:0xde
	v_add_u32_e32 v1, 32, v78
	v_lshrrev_b32_e32 v72, 3, v1
	v_and_or_b32 v72, v72, s0, v73
	v_lshlrev_b32_e32 v74, 6, v1
	v_lshlrev_b32_e32 v1, 2, v1
	v_and_or_b32 v74, v74, s1, v0
	v_lshlrev_b32_e32 v72, 10, v72
	v_and_b32_e32 v1, 32, v1
	v_bitop3_b32 v72, v74, v72, v1 bitop3:0xde
	v_add_u32_e32 v1, 48, v78
	v_lshrrev_b32_e32 v74, 3, v1
	v_and_or_b32 v73, v74, s0, v73
	v_lshlrev_b32_e32 v74, 6, v1
	v_lshlrev_b32_e32 v1, 2, v1
	v_and_or_b32 v0, v74, s1, v0
	v_lshlrev_b32_e32 v73, 10, v73
	v_and_b32_e32 v1, 32, v1
	v_bitop3_b32 v73, v0, v73, v1 bitop3:0xde
	v_lshlrev_b64 v[0:1], 12, v[68:69]
	s_lshl_b32 s0, s2, 3
	v_lshl_add_u64 v[0:1], s[6:7], 0, v[0:1]
	v_lshlrev_b32_e32 v74, 1, v79
	s_and_b32 s0, s0, 0x380
	v_lshl_add_u64 v[0:1], v[0:1], 0, v[74:75]
	s_add_i32 s9, s0, 0x100
	s_mov_b32 s10, 0x10000
	s_mov_b32 s11, 0
	s_branch .LBB0_15
